# setprio clean-up A/B in the 8-phase GEMM loops: the back-to-back s_setprio 0 / s_setprio 1 pair in the middle of every MFMA segment removed (20 sites)
# speedup vs baseline: 1.0030x; 1.0030x over previous
.LBB0_502:
	s_waitcnt vmcnt(8)
	s_add_u32 s6, s2, 0x80
	s_waitcnt lgkmcnt(0)
	s_addc_u32 s7, s3, 0
	s_and_b64 s[4:5], s[4:5], exec
	s_cselect_b32 s7, s43, s7
	s_cselect_b32 s6, s42, s6
	s_cselect_b32 s5, s1, s23
	s_cselect_b32 s4, s21, s22
	s_barrier
	s_setprio 1
	s_waitcnt lgkmcnt(0)
	v_mfma_scale_f32_16x16x128_f8f6f4 v[190:193], v[24:31], v[56:63], v[190:193], v216, v216 op_sel_hi:[0,0,0]
	v_mfma_scale_f32_16x16x128_f8f6f4 v[178:181], v[16:23], v[56:63], v[178:181], v216, v216 op_sel_hi:[0,0,0]
	v_mfma_scale_f32_16x16x128_f8f6f4 v[174:177], v[24:31], v[48:55], v[174:177], v216, v216 op_sel_hi:[0,0,0]
	v_mfma_scale_f32_16x16x128_f8f6f4 v[162:165], v[16:23], v[48:55], v[162:165], v216, v216 op_sel_hi:[0,0,0]
	v_mfma_scale_f32_16x16x128_f8f6f4 v[158:161], v[24:31], v[40:47], v[158:161], v216, v216 op_sel_hi:[0,0,0]
	v_mfma_scale_f32_16x16x128_f8f6f4 v[146:149], v[16:23], v[40:47], v[146:149], v216, v216 op_sel_hi:[0,0,0]
	v_mfma_scale_f32_16x16x128_f8f6f4 v[142:145], v[24:31], v[32:39], v[142:145], v216, v216 op_sel_hi:[0,0,0]
	v_mfma_scale_f32_16x16x128_f8f6f4 v[130:133], v[16:23], v[32:39], v[130:133], v216, v216 op_sel_hi:[0,0,0]
	v_mfma_scale_f32_16x16x128_f8f6f4 v[186:189], v[0:7], v[56:63], v[186:189], v216, v216 op_sel_hi:[0,0,0]
	v_mfma_scale_f32_16x16x128_f8f6f4 v[182:185], v[8:15], v[56:63], v[182:185], v216, v216 op_sel_hi:[0,0,0]
	v_mfma_scale_f32_16x16x128_f8f6f4 v[170:173], v[0:7], v[48:55], v[170:173], v216, v216 op_sel_hi:[0,0,0]
	v_mfma_scale_f32_16x16x128_f8f6f4 v[166:169], v[8:15], v[48:55], v[166:169], v216, v216 op_sel_hi:[0,0,0]
	v_mfma_scale_f32_16x16x128_f8f6f4 v[154:157], v[0:7], v[40:47], v[154:157], v216, v216 op_sel_hi:[0,0,0]
	v_mfma_scale_f32_16x16x128_f8f6f4 v[150:153], v[8:15], v[40:47], v[150:153], v216, v216 op_sel_hi:[0,0,0]
	v_mfma_scale_f32_16x16x128_f8f6f4 v[138:141], v[0:7], v[32:39], v[138:141], v216, v216 op_sel_hi:[0,0,0]
	v_mfma_scale_f32_16x16x128_f8f6f4 v[134:137], v[8:15], v[32:39], v[134:137], v216, v216 op_sel_hi:[0,0,0]
	s_setprio 0
	s_barrier
	s_mov_b32 m0, s16
	v_lshl_add_u64 v[246:247], s[4:5], 0, v[196:197]
	s_add_u32 s30, s4, 0x20000
	ds_read_b128 v[32:35], v242 offset:17408
	ds_read_b128 v[36:39], v245 offset:17424
	ds_read_b128 v[40:43], v242 offset:19456
	ds_read_b128 v[44:47], v245 offset:19472
	ds_read_b128 v[48:51], v242 offset:21504
	ds_read_b128 v[52:55], v245 offset:21520
	ds_read_b128 v[56:59], v242 offset:23552
	ds_read_b128 v[60:63], v245 offset:23568
	global_load_lds_dwordx4 v[246:247], off
	v_lshl_add_u64 v[248:249], s[4:5], 0, v[194:195]
	s_mov_b32 m0, s17
	s_addc_u32 s31, s5, 0
	global_load_lds_dwordx4 v[248:249], off
	v_lshl_add_u64 v[250:251], s[30:31], 0, v[196:197]
	s_mov_b32 m0, s18
	v_mov_b32_e32 v199, v113
	global_load_lds_dwordx4 v[250:251], off
	v_lshl_add_u64 v[250:251], s[30:31], 0, v[194:195]
	s_mov_b32 m0, s19
	v_lshl_add_u64 v[252:253], s[6:7], 0, v[198:199]
	global_load_lds_dwordx4 v[250:251], off
	s_mov_b32 m0, s28
	v_lshl_add_u64 v[250:251], s[6:7], 0, v[112:113]
	global_load_lds_dwordx4 v112, s[6:7]
	s_mov_b32 m0, s29
	s_nop 0
	global_load_lds_dwordx4 v198, s[6:7]
	s_waitcnt vmcnt(8)
	s_waitcnt lgkmcnt(0)
	s_barrier
	s_setprio 1
	s_waitcnt lgkmcnt(0)
	v_mfma_scale_f32_16x16x128_f8f6f4 v[126:129], v[24:31], v[32:39], v[126:129], v216, v216 op_sel_hi:[0,0,0]
	v_mfma_scale_f32_16x16x128_f8f6f4 v[114:117], v[16:23], v[32:39], v[114:117], v216, v216 op_sel_hi:[0,0,0]
	v_mfma_scale_f32_16x16x128_f8f6f4 v[108:111], v[24:31], v[40:47], v[108:111], v216, v216 op_sel_hi:[0,0,0]
	v_mfma_scale_f32_16x16x128_f8f6f4 v[96:99], v[16:23], v[40:47], v[96:99], v216, v216 op_sel_hi:[0,0,0]
	v_mfma_scale_f32_16x16x128_f8f6f4 v[92:95], v[24:31], v[48:55], v[92:95], v216, v216 op_sel_hi:[0,0,0]
	v_mfma_scale_f32_16x16x128_f8f6f4 v[80:83], v[16:23], v[48:55], v[80:83], v216, v216 op_sel_hi:[0,0,0]
	v_mfma_scale_f32_16x16x128_f8f6f4 v[76:79], v[24:31], v[56:63], v[76:79], v216, v216 op_sel_hi:[0,0,0]
	v_mfma_scale_f32_16x16x128_f8f6f4 v[68:71], v[16:23], v[56:63], v[68:71], v216, v216 op_sel_hi:[0,0,0]
	v_mfma_scale_f32_16x16x128_f8f6f4 v[122:125], v[0:7], v[32:39], v[122:125], v216, v216 op_sel_hi:[0,0,0]
	v_mfma_scale_f32_16x16x128_f8f6f4 v[118:121], v[8:15], v[32:39], v[118:121], v216, v216 op_sel_hi:[0,0,0]
	v_mfma_scale_f32_16x16x128_f8f6f4 v[104:107], v[0:7], v[40:47], v[104:107], v216, v216 op_sel_hi:[0,0,0]
	v_mfma_scale_f32_16x16x128_f8f6f4 v[100:103], v[8:15], v[40:47], v[100:103], v216, v216 op_sel_hi:[0,0,0]
	v_mfma_scale_f32_16x16x128_f8f6f4 v[88:91], v[0:7], v[48:55], v[88:91], v216, v216 op_sel_hi:[0,0,0]
	v_mfma_scale_f32_16x16x128_f8f6f4 v[84:87], v[8:15], v[48:55], v[84:87], v216, v216 op_sel_hi:[0,0,0]
	v_mfma_scale_f32_16x16x128_f8f6f4 v[72:75], v[0:7], v[56:63], v[72:75], v216, v216 op_sel_hi:[0,0,0]
	v_mfma_scale_f32_16x16x128_f8f6f4 v[64:67], v[8:15], v[56:63], v[64:67], v216, v216 op_sel_hi:[0,0,0]
	s_setprio 0
	s_barrier
	ds_read_b128 v[4:7], v236
	ds_read_b128 v[8:11], v237
	ds_read_b128 v[0:3], v228
	ds_read_b128 v[16:19], v229
	ds_read_b128 v[12:15], v238
	ds_read_b128 v[20:23], v239
	ds_read_b128 v[24:27], v240
	ds_read_b128 v[28:31], v241
	s_mov_b32 m0, s58
	v_lshl_add_u64 v[210:211], s[6:7], 0, v[210:211]
	ds_read_b128 v[32:35], v242 offset:33792
	ds_read_b128 v[36:39], v245 offset:33808
	ds_read_b128 v[40:43], v242 offset:35840
	ds_read_b128 v[44:47], v245 offset:35856
	ds_read_b128 v[48:51], v242 offset:37888
	ds_read_b128 v[52:55], v245 offset:37904
	ds_read_b128 v[56:59], v242 offset:39936
	ds_read_b128 v[60:63], v245 offset:39952
	global_load_lds_dwordx4 v[210:211], off
	v_lshl_add_u64 v[208:209], s[6:7], 0, v[208:209]
	s_mov_b32 m0, s59
	s_nop 0
	global_load_lds_dwordx4 v[208:209], off
	s_waitcnt vmcnt(8)
	s_waitcnt lgkmcnt(0)
	s_barrier
	s_setprio 1
	s_waitcnt lgkmcnt(0)
	v_mfma_scale_f32_16x16x128_f8f6f4 v[190:193], v[0:7], v[32:39], v[190:193], v216, v216 op_sel_hi:[0,0,0]
	v_mfma_scale_f32_16x16x128_f8f6f4 v[178:181], v[8:15], v[32:39], v[178:181], v216, v216 op_sel_hi:[0,0,0]
	v_mfma_scale_f32_16x16x128_f8f6f4 v[174:177], v[0:7], v[40:47], v[174:177], v216, v216 op_sel_hi:[0,0,0]
	v_mfma_scale_f32_16x16x128_f8f6f4 v[162:165], v[8:15], v[40:47], v[162:165], v216, v216 op_sel_hi:[0,0,0]
	v_mfma_scale_f32_16x16x128_f8f6f4 v[158:161], v[0:7], v[48:55], v[158:161], v216, v216 op_sel_hi:[0,0,0]
	v_mfma_scale_f32_16x16x128_f8f6f4 v[146:149], v[8:15], v[48:55], v[146:149], v216, v216 op_sel_hi:[0,0,0]
	v_mfma_scale_f32_16x16x128_f8f6f4 v[142:145], v[0:7], v[56:63], v[142:145], v216, v216 op_sel_hi:[0,0,0]
	v_mfma_scale_f32_16x16x128_f8f6f4 v[130:133], v[8:15], v[56:63], v[130:133], v216, v216 op_sel_hi:[0,0,0]
	v_mfma_scale_f32_16x16x128_f8f6f4 v[186:189], v[16:23], v[32:39], v[186:189], v216, v216 op_sel_hi:[0,0,0]
	v_mfma_scale_f32_16x16x128_f8f6f4 v[182:185], v[24:31], v[32:39], v[182:185], v216, v216 op_sel_hi:[0,0,0]
	v_mfma_scale_f32_16x16x128_f8f6f4 v[170:173], v[16:23], v[40:47], v[170:173], v216, v216 op_sel_hi:[0,0,0]
	v_mfma_scale_f32_16x16x128_f8f6f4 v[166:169], v[24:31], v[40:47], v[166:169], v216, v216 op_sel_hi:[0,0,0]
	v_mfma_scale_f32_16x16x128_f8f6f4 v[154:157], v[16:23], v[48:55], v[154:157], v216, v216 op_sel_hi:[0,0,0]
	v_mfma_scale_f32_16x16x128_f8f6f4 v[150:153], v[24:31], v[48:55], v[150:153], v216, v216 op_sel_hi:[0,0,0]
	v_mfma_scale_f32_16x16x128_f8f6f4 v[138:141], v[16:23], v[56:63], v[138:141], v216, v216 op_sel_hi:[0,0,0]
	v_mfma_scale_f32_16x16x128_f8f6f4 v[134:137], v[24:31], v[56:63], v[134:137], v216, v216 op_sel_hi:[0,0,0]
	s_setprio 0
	s_barrier
	s_mov_b32 m0, s65
	v_lshl_add_u64 v[208:209], v[246:247], 0, s[26:27]
	s_add_u32 s4, s4, 0x20080
	ds_read_b128 v[32:35], v242 offset:50176
	ds_read_b128 v[36:39], v245 offset:50192
	ds_read_b128 v[40:43], v242 offset:52224
	ds_read_b128 v[44:47], v245 offset:52240
	ds_read_b128 v[48:51], v242 offset:54272
	ds_read_b128 v[52:55], v245 offset:54288
	ds_read_b128 v[56:59], v242 offset:56320
	ds_read_b128 v[60:63], v245 offset:56336
	global_load_lds_dwordx4 v[208:209], off
	v_lshl_add_u64 v[208:209], v[248:249], 0, s[26:27]
	s_mov_b32 m0, s66
	s_addc_u32 s5, s5, 0
	global_load_lds_dwordx4 v[208:209], off
	v_lshl_add_u64 v[208:209], s[4:5], 0, v[196:197]
	s_mov_b32 m0, s69
	s_nop 0
	global_load_lds_dwordx4 v[208:209], off
	v_lshl_add_u64 v[208:209], s[4:5], 0, v[194:195]
	s_mov_b32 m0, s70
	s_nop 0
	global_load_lds_dwordx4 v[208:209], off
	v_lshl_add_u64 v[208:209], v[250:251], 0, s[26:27]
	s_mov_b32 m0, s67
	s_nop 0
	global_load_lds_dwordx4 v[208:209], off
	v_lshl_add_u64 v[208:209], v[252:253], 0, s[26:27]
	s_mov_b32 m0, s68
	s_nop 0
	global_load_lds_dwordx4 v[208:209], off
	s_waitcnt vmcnt(8)
	s_waitcnt lgkmcnt(0)
	s_barrier
	s_setprio 1
	s_waitcnt lgkmcnt(0)
	v_mfma_scale_f32_16x16x128_f8f6f4 v[126:129], v[0:7], v[32:39], v[126:129], v216, v216 op_sel_hi:[0,0,0]
	v_mfma_scale_f32_16x16x128_f8f6f4 v[114:117], v[8:15], v[32:39], v[114:117], v216, v216 op_sel_hi:[0,0,0]
	v_mfma_scale_f32_16x16x128_f8f6f4 v[108:111], v[0:7], v[40:47], v[108:111], v216, v216 op_sel_hi:[0,0,0]
	v_mfma_scale_f32_16x16x128_f8f6f4 v[96:99], v[8:15], v[40:47], v[96:99], v216, v216 op_sel_hi:[0,0,0]
	v_mfma_scale_f32_16x16x128_f8f6f4 v[92:95], v[0:7], v[48:55], v[92:95], v216, v216 op_sel_hi:[0,0,0]
	v_mfma_scale_f32_16x16x128_f8f6f4 v[80:83], v[8:15], v[48:55], v[80:83], v216, v216 op_sel_hi:[0,0,0]
	v_mfma_scale_f32_16x16x128_f8f6f4 v[76:79], v[0:7], v[56:63], v[76:79], v216, v216 op_sel_hi:[0,0,0]
	v_mfma_scale_f32_16x16x128_f8f6f4 v[68:71], v[8:15], v[56:63], v[68:71], v216, v216 op_sel_hi:[0,0,0]
	v_mfma_scale_f32_16x16x128_f8f6f4 v[122:125], v[16:23], v[32:39], v[122:125], v216, v216 op_sel_hi:[0,0,0]
	v_mfma_scale_f32_16x16x128_f8f6f4 v[118:121], v[24:31], v[32:39], v[118:121], v216, v216 op_sel_hi:[0,0,0]
	v_mfma_scale_f32_16x16x128_f8f6f4 v[104:107], v[16:23], v[40:47], v[104:107], v216, v216 op_sel_hi:[0,0,0]
	v_mfma_scale_f32_16x16x128_f8f6f4 v[100:103], v[24:31], v[40:47], v[100:103], v216, v216 op_sel_hi:[0,0,0]
	v_mfma_scale_f32_16x16x128_f8f6f4 v[88:91], v[16:23], v[48:55], v[88:91], v216, v216 op_sel_hi:[0,0,0]
	v_mfma_scale_f32_16x16x128_f8f6f4 v[84:87], v[24:31], v[48:55], v[84:87], v216, v216 op_sel_hi:[0,0,0]
	v_mfma_scale_f32_16x16x128_f8f6f4 v[72:75], v[16:23], v[56:63], v[72:75], v216, v216 op_sel_hi:[0,0,0]
	v_mfma_scale_f32_16x16x128_f8f6f4 v[64:67], v[24:31], v[56:63], v[64:67], v216, v216 op_sel_hi:[0,0,0]
	s_setprio 0
	s_barrier
	s_add_i32 s24, s24, 2
	s_add_u32 s22, s22, 0x100
	s_addc_u32 s23, s23, 0
	s_add_u32 s2, s2, 0x100
	s_addc_u32 s3, s3, 0
	s_cmp_gt_u32 s24, 5
	s_cbranch_scc1 .LBB0_505

.LBB0_586:
	s_waitcnt vmcnt(8)
	s_add_u32 s4, s0, 0x80
	s_waitcnt lgkmcnt(0)
	s_addc_u32 s5, s1, 0
	s_and_b64 s[2:3], s[2:3], exec
	s_cselect_b32 s5, s47, s5
	s_cselect_b32 s4, s46, s4
	s_cselect_b32 s3, s21, s24
	s_cselect_b32 s2, s22, s23
	s_barrier
	s_setprio 1
	s_waitcnt lgkmcnt(0)
	v_mfma_f32_16x16x32_bf16 v[126:129], v[146:149], v[186:189], v[126:129]
	v_mfma_f32_16x16x32_bf16 v[122:125], v[154:157], v[186:189], v[122:125]
	v_mfma_f32_16x16x32_bf16 v[108:111], v[146:149], v[178:181], v[108:111]
	v_mfma_f32_16x16x32_bf16 v[104:107], v[154:157], v[178:181], v[104:107]
	v_mfma_f32_16x16x32_bf16 v[92:95], v[146:149], v[170:173], v[92:95]
	v_mfma_f32_16x16x32_bf16 v[88:91], v[154:157], v[170:173], v[88:91]
	v_mfma_f32_16x16x32_bf16 v[76:79], v[146:149], v[162:165], v[76:79]
	v_mfma_f32_16x16x32_bf16 v[72:75], v[154:157], v[162:165], v[72:75]
	v_mfma_f32_16x16x32_bf16 v[126:129], v[150:153], v[190:193], v[126:129]
	v_mfma_f32_16x16x32_bf16 v[122:125], v[158:161], v[190:193], v[122:125]
	v_mfma_f32_16x16x32_bf16 v[108:111], v[150:153], v[182:185], v[108:111]
	v_mfma_f32_16x16x32_bf16 v[104:107], v[158:161], v[182:185], v[104:107]
	v_mfma_f32_16x16x32_bf16 v[92:95], v[150:153], v[174:177], v[92:95]
	v_mfma_f32_16x16x32_bf16 v[88:91], v[158:161], v[174:177], v[88:91]
	v_mfma_f32_16x16x32_bf16 v[76:79], v[150:153], v[166:169], v[76:79]
	v_mfma_f32_16x16x32_bf16 v[72:75], v[158:161], v[166:169], v[72:75]
	v_mfma_f32_16x16x32_bf16 v[118:121], v[130:133], v[186:189], v[118:121]
	v_mfma_f32_16x16x32_bf16 v[114:117], v[138:141], v[186:189], v[114:117]
	v_mfma_f32_16x16x32_bf16 v[100:103], v[130:133], v[178:181], v[100:103]
	v_mfma_f32_16x16x32_bf16 v[96:99], v[138:141], v[178:181], v[96:99]
	v_mfma_f32_16x16x32_bf16 v[84:87], v[130:133], v[170:173], v[84:87]
	v_mfma_f32_16x16x32_bf16 v[80:83], v[138:141], v[170:173], v[80:83]
	v_mfma_f32_16x16x32_bf16 v[68:71], v[130:133], v[162:165], v[68:71]
	v_mfma_f32_16x16x32_bf16 v[64:67], v[138:141], v[162:165], v[64:67]
	v_mfma_f32_16x16x32_bf16 v[118:121], v[134:137], v[190:193], v[118:121]
	v_mfma_f32_16x16x32_bf16 v[114:117], v[142:145], v[190:193], v[114:117]
	v_mfma_f32_16x16x32_bf16 v[100:103], v[134:137], v[182:185], v[100:103]
	v_mfma_f32_16x16x32_bf16 v[96:99], v[142:145], v[182:185], v[96:99]
	v_mfma_f32_16x16x32_bf16 v[84:87], v[134:137], v[174:177], v[84:87]
	v_mfma_f32_16x16x32_bf16 v[80:83], v[142:145], v[174:177], v[80:83]
	v_mfma_f32_16x16x32_bf16 v[68:71], v[134:137], v[166:169], v[68:71]
	v_mfma_f32_16x16x32_bf16 v[64:67], v[142:145], v[166:169], v[64:67]
	s_setprio 0
	s_barrier
	s_mov_b32 m0, s19
	v_lshl_add_u64 v[232:233], s[2:3], 0, v[194:195]
	s_add_u32 s38, s2, 0x40000
	ds_read_b128 v[162:165], v229 offset:17408
	ds_read_b128 v[166:169], v229 offset:18432
	ds_read_b128 v[170:173], v229 offset:19456
	ds_read_b128 v[174:177], v229 offset:20480
	ds_read_b128 v[178:181], v229 offset:21504
	ds_read_b128 v[182:185], v229 offset:22528
	ds_read_b128 v[186:189], v229 offset:23552
	ds_read_b128 v[190:193], v229 offset:24576
	global_load_lds_dwordx4 v[232:233], off
	v_lshl_add_u64 v[234:235], s[2:3], 0, v[196:197]
	s_mov_b32 m0, s28
	s_addc_u32 s39, s3, 0
	global_load_lds_dwordx4 v[234:235], off
	v_lshl_add_u64 v[236:237], s[38:39], 0, v[194:195]
	s_mov_b32 m0, s29
	v_mov_b32_e32 v199, v113
	global_load_lds_dwordx4 v[236:237], off
	v_lshl_add_u64 v[236:237], s[38:39], 0, v[196:197]
	s_mov_b32 m0, s65
	v_lshl_add_u64 v[238:239], s[4:5], 0, v[198:199]
	global_load_lds_dwordx4 v[236:237], off
	s_mov_b32 m0, s66
	v_lshl_add_u64 v[236:237], s[4:5], 0, v[112:113]
	global_load_lds_dwordx4 v112, s[4:5]
	s_mov_b32 m0, s67
	s_nop 0
	global_load_lds_dwordx4 v198, s[4:5]
	s_waitcnt vmcnt(8)
	s_waitcnt lgkmcnt(0)
	s_barrier
	s_setprio 1
	s_waitcnt lgkmcnt(0)
	v_mfma_f32_16x16x32_bf16 v[60:63], v[146:149], v[162:165], v[60:63]
	v_mfma_f32_16x16x32_bf16 v[56:59], v[154:157], v[162:165], v[56:59]
	v_mfma_f32_16x16x32_bf16 v[44:47], v[146:149], v[170:173], v[44:47]
	v_mfma_f32_16x16x32_bf16 v[40:43], v[154:157], v[170:173], v[40:43]
	v_mfma_f32_16x16x32_bf16 v[28:31], v[146:149], v[178:181], v[28:31]
	v_mfma_f32_16x16x32_bf16 v[24:27], v[154:157], v[178:181], v[24:27]
	v_mfma_f32_16x16x32_bf16 v[12:15], v[146:149], v[186:189], v[12:15]
	v_mfma_f32_16x16x32_bf16 v[8:11], v[154:157], v[186:189], v[8:11]
	v_mfma_f32_16x16x32_bf16 v[60:63], v[150:153], v[166:169], v[60:63]
	v_mfma_f32_16x16x32_bf16 v[56:59], v[158:161], v[166:169], v[56:59]
	v_mfma_f32_16x16x32_bf16 v[44:47], v[150:153], v[174:177], v[44:47]
	v_mfma_f32_16x16x32_bf16 v[40:43], v[158:161], v[174:177], v[40:43]
	v_mfma_f32_16x16x32_bf16 v[28:31], v[150:153], v[182:185], v[28:31]
	v_mfma_f32_16x16x32_bf16 v[24:27], v[158:161], v[182:185], v[24:27]
	v_mfma_f32_16x16x32_bf16 v[12:15], v[150:153], v[190:193], v[12:15]
	v_mfma_f32_16x16x32_bf16 v[8:11], v[158:161], v[190:193], v[8:11]
	v_mfma_f32_16x16x32_bf16 v[52:55], v[130:133], v[162:165], v[52:55]
	v_mfma_f32_16x16x32_bf16 v[48:51], v[138:141], v[162:165], v[48:51]
	v_mfma_f32_16x16x32_bf16 v[36:39], v[130:133], v[170:173], v[36:39]
	v_mfma_f32_16x16x32_bf16 v[32:35], v[138:141], v[170:173], v[32:35]
	v_mfma_f32_16x16x32_bf16 v[20:23], v[130:133], v[178:181], v[20:23]
	v_mfma_f32_16x16x32_bf16 v[16:19], v[138:141], v[178:181], v[16:19]
	v_mfma_f32_16x16x32_bf16 v[4:7], v[130:133], v[186:189], v[4:7]
	v_mfma_f32_16x16x32_bf16 v[0:3], v[138:141], v[186:189], v[0:3]
	v_mfma_f32_16x16x32_bf16 v[52:55], v[134:137], v[166:169], v[52:55]
	v_mfma_f32_16x16x32_bf16 v[48:51], v[142:145], v[166:169], v[48:51]
	v_mfma_f32_16x16x32_bf16 v[36:39], v[134:137], v[174:177], v[36:39]
	v_mfma_f32_16x16x32_bf16 v[32:35], v[142:145], v[174:177], v[32:35]
	v_mfma_f32_16x16x32_bf16 v[20:23], v[134:137], v[182:185], v[20:23]
	v_mfma_f32_16x16x32_bf16 v[16:19], v[142:145], v[182:185], v[16:19]
	v_mfma_f32_16x16x32_bf16 v[4:7], v[134:137], v[190:193], v[4:7]
	v_mfma_f32_16x16x32_bf16 v[0:3], v[142:145], v[190:193], v[0:3]
	s_setprio 0
	s_barrier
	s_add_i32 s31, 0, 0x18400
	s_add_i32 s35, 0, 0x1c400
	v_add_u32_e32 v142, s31, v228
	v_add_u32_e32 v158, s35, v228
	ds_read_b128 v[130:133], v142
	ds_read_b128 v[134:137], v142 offset:1024
	ds_read_b128 v[138:141], v142 offset:2048
	ds_read_b128 v[142:145], v142 offset:3072
	ds_read_b128 v[146:149], v158
	ds_read_b128 v[150:153], v158 offset:1024
	ds_read_b128 v[154:157], v158 offset:2048
	ds_read_b128 v[158:161], v158 offset:3072
	s_mov_b32 m0, s68
	v_lshl_add_u64 v[210:211], s[4:5], 0, v[210:211]
	ds_read_b128 v[162:165], v229 offset:33792
	ds_read_b128 v[166:169], v229 offset:34816
	ds_read_b128 v[170:173], v229 offset:35840
	ds_read_b128 v[174:177], v229 offset:36864
	ds_read_b128 v[178:181], v229 offset:37888
	ds_read_b128 v[182:185], v229 offset:38912
	ds_read_b128 v[186:189], v229 offset:39936
	ds_read_b128 v[190:193], v229 offset:40960
	global_load_lds_dwordx4 v[210:211], off
	v_lshl_add_u64 v[208:209], s[4:5], 0, v[208:209]
	s_mov_b32 m0, s69
	s_nop 0
	global_load_lds_dwordx4 v[208:209], off
	s_waitcnt vmcnt(8)
	s_waitcnt lgkmcnt(0)
	s_barrier
	s_setprio 1
	s_waitcnt lgkmcnt(0)
	v_mfma_f32_16x16x32_bf16 v[126:129], v[130:133], v[162:165], v[126:129]
	v_mfma_f32_16x16x32_bf16 v[122:125], v[138:141], v[162:165], v[122:125]
	v_mfma_f32_16x16x32_bf16 v[108:111], v[130:133], v[170:173], v[108:111]
	v_mfma_f32_16x16x32_bf16 v[104:107], v[138:141], v[170:173], v[104:107]
	v_mfma_f32_16x16x32_bf16 v[92:95], v[130:133], v[178:181], v[92:95]
	v_mfma_f32_16x16x32_bf16 v[88:91], v[138:141], v[178:181], v[88:91]
	v_mfma_f32_16x16x32_bf16 v[76:79], v[130:133], v[186:189], v[76:79]
	v_mfma_f32_16x16x32_bf16 v[72:75], v[138:141], v[186:189], v[72:75]
	v_mfma_f32_16x16x32_bf16 v[126:129], v[134:137], v[166:169], v[126:129]
	v_mfma_f32_16x16x32_bf16 v[122:125], v[142:145], v[166:169], v[122:125]
	v_mfma_f32_16x16x32_bf16 v[108:111], v[134:137], v[174:177], v[108:111]
	v_mfma_f32_16x16x32_bf16 v[104:107], v[142:145], v[174:177], v[104:107]
	v_mfma_f32_16x16x32_bf16 v[92:95], v[134:137], v[182:185], v[92:95]
	v_mfma_f32_16x16x32_bf16 v[88:91], v[142:145], v[182:185], v[88:91]
	v_mfma_f32_16x16x32_bf16 v[76:79], v[134:137], v[190:193], v[76:79]
	v_mfma_f32_16x16x32_bf16 v[72:75], v[142:145], v[190:193], v[72:75]
	v_mfma_f32_16x16x32_bf16 v[118:121], v[146:149], v[162:165], v[118:121]
	v_mfma_f32_16x16x32_bf16 v[114:117], v[154:157], v[162:165], v[114:117]
	v_mfma_f32_16x16x32_bf16 v[100:103], v[146:149], v[170:173], v[100:103]
	v_mfma_f32_16x16x32_bf16 v[96:99], v[154:157], v[170:173], v[96:99]
	v_mfma_f32_16x16x32_bf16 v[84:87], v[146:149], v[178:181], v[84:87]
	v_mfma_f32_16x16x32_bf16 v[80:83], v[154:157], v[178:181], v[80:83]
	v_mfma_f32_16x16x32_bf16 v[68:71], v[146:149], v[186:189], v[68:71]
	v_mfma_f32_16x16x32_bf16 v[64:67], v[154:157], v[186:189], v[64:67]
	v_mfma_f32_16x16x32_bf16 v[118:121], v[150:153], v[166:169], v[118:121]
	v_mfma_f32_16x16x32_bf16 v[114:117], v[158:161], v[166:169], v[114:117]
	v_mfma_f32_16x16x32_bf16 v[100:103], v[150:153], v[174:177], v[100:103]
	v_mfma_f32_16x16x32_bf16 v[96:99], v[158:161], v[174:177], v[96:99]
	v_mfma_f32_16x16x32_bf16 v[84:87], v[150:153], v[182:185], v[84:87]
	v_mfma_f32_16x16x32_bf16 v[80:83], v[158:161], v[182:185], v[80:83]
	v_mfma_f32_16x16x32_bf16 v[68:71], v[150:153], v[190:193], v[68:71]
	v_mfma_f32_16x16x32_bf16 v[64:67], v[158:161], v[190:193], v[64:67]
	s_setprio 0
	s_barrier
	s_add_i32 s4, s31, s17
	v_lshl_add_u64 v[208:209], v[232:233], 0, s[26:27]
	s_mov_b32 m0, s4
	ds_read_b128 v[162:165], v229 offset:50176
	ds_read_b128 v[166:169], v229 offset:51200
	ds_read_b128 v[170:173], v229 offset:52224
	ds_read_b128 v[174:177], v229 offset:53248
	ds_read_b128 v[178:181], v229 offset:54272
	ds_read_b128 v[182:185], v229 offset:55296
	ds_read_b128 v[186:189], v229 offset:56320
	ds_read_b128 v[190:193], v229 offset:57344
	global_load_lds_dwordx4 v[208:209], off
	s_add_i32 m0, s4, 0x2000
	s_add_u32 s2, s2, 0x40080
	v_lshl_add_u64 v[208:209], v[234:235], 0, s[26:27]
	s_addc_u32 s3, s3, 0
	s_add_i32 s4, s35, s17
	global_load_lds_dwordx4 v[208:209], off
	v_lshl_add_u64 v[208:209], s[2:3], 0, v[194:195]
	s_mov_b32 m0, s4
	s_nop 0
	global_load_lds_dwordx4 v[208:209], off
	v_lshl_add_u64 v[208:209], s[2:3], 0, v[196:197]
	s_add_i32 m0, s4, 0x2000
	s_nop 0
	global_load_lds_dwordx4 v[208:209], off
	v_lshl_add_u64 v[208:209], v[236:237], 0, s[26:27]
	s_mov_b32 m0, s74
	s_nop 0
	global_load_lds_dwordx4 v[208:209], off
	v_lshl_add_u64 v[208:209], v[238:239], 0, s[26:27]
	s_mov_b32 m0, s75
	s_nop 0
	global_load_lds_dwordx4 v[208:209], off
	s_waitcnt vmcnt(8)
	s_waitcnt lgkmcnt(0)
	s_barrier
	s_setprio 1
	s_waitcnt lgkmcnt(0)
	v_mfma_f32_16x16x32_bf16 v[60:63], v[130:133], v[162:165], v[60:63]
	v_mfma_f32_16x16x32_bf16 v[56:59], v[138:141], v[162:165], v[56:59]
	v_mfma_f32_16x16x32_bf16 v[44:47], v[130:133], v[170:173], v[44:47]
	v_mfma_f32_16x16x32_bf16 v[40:43], v[138:141], v[170:173], v[40:43]
	v_mfma_f32_16x16x32_bf16 v[28:31], v[130:133], v[178:181], v[28:31]
	v_mfma_f32_16x16x32_bf16 v[24:27], v[138:141], v[178:181], v[24:27]
	v_mfma_f32_16x16x32_bf16 v[12:15], v[130:133], v[186:189], v[12:15]
	v_mfma_f32_16x16x32_bf16 v[8:11], v[138:141], v[186:189], v[8:11]
	v_mfma_f32_16x16x32_bf16 v[60:63], v[134:137], v[166:169], v[60:63]
	v_mfma_f32_16x16x32_bf16 v[56:59], v[142:145], v[166:169], v[56:59]
	v_mfma_f32_16x16x32_bf16 v[44:47], v[134:137], v[174:177], v[44:47]
	v_mfma_f32_16x16x32_bf16 v[40:43], v[142:145], v[174:177], v[40:43]
	v_mfma_f32_16x16x32_bf16 v[28:31], v[134:137], v[182:185], v[28:31]
	v_mfma_f32_16x16x32_bf16 v[24:27], v[142:145], v[182:185], v[24:27]
	v_mfma_f32_16x16x32_bf16 v[12:15], v[134:137], v[190:193], v[12:15]
	v_mfma_f32_16x16x32_bf16 v[8:11], v[142:145], v[190:193], v[8:11]
	v_mfma_f32_16x16x32_bf16 v[52:55], v[146:149], v[162:165], v[52:55]
	v_mfma_f32_16x16x32_bf16 v[48:51], v[154:157], v[162:165], v[48:51]
	v_mfma_f32_16x16x32_bf16 v[36:39], v[146:149], v[170:173], v[36:39]
	v_mfma_f32_16x16x32_bf16 v[32:35], v[154:157], v[170:173], v[32:35]
	v_mfma_f32_16x16x32_bf16 v[20:23], v[146:149], v[178:181], v[20:23]
	v_mfma_f32_16x16x32_bf16 v[16:19], v[154:157], v[178:181], v[16:19]
	v_mfma_f32_16x16x32_bf16 v[4:7], v[146:149], v[186:189], v[4:7]
	v_mfma_f32_16x16x32_bf16 v[0:3], v[154:157], v[186:189], v[0:3]
	v_mfma_f32_16x16x32_bf16 v[52:55], v[150:153], v[166:169], v[52:55]
	v_mfma_f32_16x16x32_bf16 v[48:51], v[158:161], v[166:169], v[48:51]
	v_mfma_f32_16x16x32_bf16 v[36:39], v[150:153], v[174:177], v[36:39]
	v_mfma_f32_16x16x32_bf16 v[32:35], v[158:161], v[174:177], v[32:35]
	v_mfma_f32_16x16x32_bf16 v[20:23], v[150:153], v[182:185], v[20:23]
	v_mfma_f32_16x16x32_bf16 v[16:19], v[158:161], v[182:185], v[16:19]
	v_mfma_f32_16x16x32_bf16 v[4:7], v[150:153], v[190:193], v[4:7]
	v_mfma_f32_16x16x32_bf16 v[0:3], v[158:161], v[190:193], v[0:3]
	s_setprio 0
	s_barrier
	s_add_i32 s30, s30, 2
	s_add_u32 s23, s23, 0x100
	s_addc_u32 s24, s24, 0
	s_add_u32 s0, s0, 0x100
	s_addc_u32 s1, s1, 0
	s_cmp_gt_u32 s30, 13
	s_cbranch_scc1 .LBB0_589

.LBB0_940:
	s_waitcnt vmcnt(8)
	s_add_u32 s6, s2, 0x80
	s_waitcnt lgkmcnt(0)
	s_addc_u32 s7, s3, 0
	s_and_b64 s[4:5], s[4:5], exec
	s_cselect_b32 s7, s51, s7
	s_cselect_b32 s6, s50, s6
	s_cselect_b32 s5, s1, s23
	s_cselect_b32 s4, s21, s22
	s_barrier
	s_setprio 1
	s_waitcnt lgkmcnt(0)
	v_mfma_f32_16x16x32_bf16 v[142:145], v[146:149], v[186:189], v[142:145]
	v_mfma_f32_16x16x32_bf16 v[138:141], v[154:157], v[186:189], v[138:141]
	v_mfma_f32_16x16x32_bf16 v[126:129], v[146:149], v[178:181], v[126:129]
	v_mfma_f32_16x16x32_bf16 v[122:125], v[154:157], v[178:181], v[122:125]
	v_mfma_f32_16x16x32_bf16 v[108:111], v[146:149], v[170:173], v[108:111]
	v_mfma_f32_16x16x32_bf16 v[104:107], v[154:157], v[170:173], v[104:107]
	v_mfma_f32_16x16x32_bf16 v[92:95], v[146:149], v[162:165], v[92:95]
	v_mfma_f32_16x16x32_bf16 v[88:91], v[154:157], v[162:165], v[88:91]
	v_mfma_f32_16x16x32_bf16 v[142:145], v[150:153], v[190:193], v[142:145]
	v_mfma_f32_16x16x32_bf16 v[138:141], v[158:161], v[190:193], v[138:141]
	v_mfma_f32_16x16x32_bf16 v[126:129], v[150:153], v[182:185], v[126:129]
	v_mfma_f32_16x16x32_bf16 v[122:125], v[158:161], v[182:185], v[122:125]
	v_mfma_f32_16x16x32_bf16 v[108:111], v[150:153], v[174:177], v[108:111]
	v_mfma_f32_16x16x32_bf16 v[104:107], v[158:161], v[174:177], v[104:107]
	v_mfma_f32_16x16x32_bf16 v[92:95], v[150:153], v[166:169], v[92:95]
	v_mfma_f32_16x16x32_bf16 v[88:91], v[158:161], v[166:169], v[88:91]
	v_mfma_f32_16x16x32_bf16 v[134:137], v[60:63], v[186:189], v[134:137]
	v_mfma_f32_16x16x32_bf16 v[130:133], v[72:75], v[186:189], v[130:133]
	v_mfma_f32_16x16x32_bf16 v[118:121], v[60:63], v[178:181], v[118:121]
	v_mfma_f32_16x16x32_bf16 v[114:117], v[72:75], v[178:181], v[114:117]
	v_mfma_f32_16x16x32_bf16 v[100:103], v[60:63], v[170:173], v[100:103]
	v_mfma_f32_16x16x32_bf16 v[96:99], v[72:75], v[170:173], v[96:99]
	v_mfma_f32_16x16x32_bf16 v[84:87], v[60:63], v[162:165], v[84:87]
	v_mfma_f32_16x16x32_bf16 v[76:79], v[72:75], v[162:165], v[76:79]
	v_mfma_f32_16x16x32_bf16 v[134:137], v[64:67], v[190:193], v[134:137]
	v_mfma_f32_16x16x32_bf16 v[130:133], v[80:83], v[190:193], v[130:133]
	v_mfma_f32_16x16x32_bf16 v[118:121], v[64:67], v[182:185], v[118:121]
	v_mfma_f32_16x16x32_bf16 v[114:117], v[80:83], v[182:185], v[114:117]
	v_mfma_f32_16x16x32_bf16 v[100:103], v[64:67], v[174:177], v[100:103]
	v_mfma_f32_16x16x32_bf16 v[96:99], v[80:83], v[174:177], v[96:99]
	v_mfma_f32_16x16x32_bf16 v[84:87], v[64:67], v[166:169], v[84:87]
	v_mfma_f32_16x16x32_bf16 v[76:79], v[80:83], v[166:169], v[76:79]
	s_setprio 0
	s_barrier
	s_mov_b32 m0, s29
	v_lshl_add_u64 v[232:233], s[4:5], 0, v[194:195]
	s_add_u32 s30, s4, 0x40000
	ds_read_b128 v[162:165], v229 offset:17408
	ds_read_b128 v[166:169], v229 offset:18432
	ds_read_b128 v[170:173], v229 offset:19456
	ds_read_b128 v[174:177], v229 offset:20480
	ds_read_b128 v[178:181], v229 offset:21504
	ds_read_b128 v[182:185], v229 offset:22528
	ds_read_b128 v[186:189], v229 offset:23552
	ds_read_b128 v[190:193], v229 offset:24576
	global_load_lds_dwordx4 v[232:233], off
	v_lshl_add_u64 v[234:235], s[4:5], 0, v[196:197]
	s_mov_b32 m0, s70
	s_addc_u32 s31, s5, 0
	global_load_lds_dwordx4 v[234:235], off
	v_lshl_add_u64 v[236:237], s[30:31], 0, v[194:195]
	s_mov_b32 m0, s71
	v_mov_b32_e32 v201, v113
	global_load_lds_dwordx4 v[236:237], off
	v_lshl_add_u64 v[236:237], s[30:31], 0, v[196:197]
	s_mov_b32 m0, s72
	v_lshl_add_u64 v[238:239], s[6:7], 0, v[200:201]
	global_load_lds_dwordx4 v[236:237], off
	s_mov_b32 m0, s73
	v_lshl_add_u64 v[236:237], s[6:7], 0, v[112:113]
	global_load_lds_dwordx4 v112, s[6:7]
	s_mov_b32 m0, s74
	s_nop 0
	global_load_lds_dwordx4 v200, s[6:7]
	s_waitcnt vmcnt(8)
	s_waitcnt lgkmcnt(0)
	s_barrier
	s_setprio 1
	s_waitcnt lgkmcnt(0)
	v_mfma_f32_16x16x32_bf16 v[68:71], v[146:149], v[162:165], v[68:71]
	v_mfma_f32_16x16x32_bf16 v[56:59], v[154:157], v[162:165], v[56:59]
	v_mfma_f32_16x16x32_bf16 v[44:47], v[146:149], v[170:173], v[44:47]
	v_mfma_f32_16x16x32_bf16 v[40:43], v[154:157], v[170:173], v[40:43]
	v_mfma_f32_16x16x32_bf16 v[28:31], v[146:149], v[178:181], v[28:31]
	v_mfma_f32_16x16x32_bf16 v[24:27], v[154:157], v[178:181], v[24:27]
	v_mfma_f32_16x16x32_bf16 v[12:15], v[146:149], v[186:189], v[12:15]
	v_mfma_f32_16x16x32_bf16 v[8:11], v[154:157], v[186:189], v[8:11]
	v_mfma_f32_16x16x32_bf16 v[68:71], v[150:153], v[166:169], v[68:71]
	v_mfma_f32_16x16x32_bf16 v[56:59], v[158:161], v[166:169], v[56:59]
	v_mfma_f32_16x16x32_bf16 v[44:47], v[150:153], v[174:177], v[44:47]
	v_mfma_f32_16x16x32_bf16 v[40:43], v[158:161], v[174:177], v[40:43]
	v_mfma_f32_16x16x32_bf16 v[28:31], v[150:153], v[182:185], v[28:31]
	v_mfma_f32_16x16x32_bf16 v[24:27], v[158:161], v[182:185], v[24:27]
	v_mfma_f32_16x16x32_bf16 v[12:15], v[150:153], v[190:193], v[12:15]
	v_mfma_f32_16x16x32_bf16 v[8:11], v[158:161], v[190:193], v[8:11]
	v_mfma_f32_16x16x32_bf16 v[52:55], v[60:63], v[162:165], v[52:55]
	v_mfma_f32_16x16x32_bf16 v[48:51], v[72:75], v[162:165], v[48:51]
	v_mfma_f32_16x16x32_bf16 v[36:39], v[60:63], v[170:173], v[36:39]
	v_mfma_f32_16x16x32_bf16 v[32:35], v[72:75], v[170:173], v[32:35]
	v_mfma_f32_16x16x32_bf16 v[20:23], v[60:63], v[178:181], v[20:23]
	v_mfma_f32_16x16x32_bf16 v[16:19], v[72:75], v[178:181], v[16:19]
	v_mfma_f32_16x16x32_bf16 v[4:7], v[60:63], v[186:189], v[4:7]
	v_mfma_f32_16x16x32_bf16 v[0:3], v[72:75], v[186:189], v[0:3]
	v_mfma_f32_16x16x32_bf16 v[52:55], v[64:67], v[166:169], v[52:55]
	v_mfma_f32_16x16x32_bf16 v[48:51], v[80:83], v[166:169], v[48:51]
	v_mfma_f32_16x16x32_bf16 v[36:39], v[64:67], v[174:177], v[36:39]
	v_mfma_f32_16x16x32_bf16 v[32:35], v[80:83], v[174:177], v[32:35]
	v_mfma_f32_16x16x32_bf16 v[20:23], v[64:67], v[182:185], v[20:23]
	v_mfma_f32_16x16x32_bf16 v[16:19], v[80:83], v[182:185], v[16:19]
	v_mfma_f32_16x16x32_bf16 v[4:7], v[64:67], v[190:193], v[4:7]
	v_mfma_f32_16x16x32_bf16 v[0:3], v[80:83], v[190:193], v[0:3]
	s_setprio 0
	s_barrier
	s_add_i32 s30, 0, 0x18400
	s_add_i32 s31, 0, 0x1c400
	v_add_u32_e32 v80, s30, v228
	v_add_u32_e32 v158, s31, v228
	ds_read_b128 v[60:63], v80
	ds_read_b128 v[64:67], v80 offset:1024
	ds_read_b128 v[72:75], v80 offset:2048
	ds_read_b128 v[80:83], v80 offset:3072
	ds_read_b128 v[146:149], v158
	ds_read_b128 v[150:153], v158 offset:1024
	ds_read_b128 v[154:157], v158 offset:2048
	ds_read_b128 v[158:161], v158 offset:3072
	s_mov_b32 m0, s75
	v_lshl_add_u64 v[210:211], s[6:7], 0, v[210:211]
	ds_read_b128 v[162:165], v229 offset:33792
	ds_read_b128 v[166:169], v229 offset:34816
	ds_read_b128 v[170:173], v229 offset:35840
	ds_read_b128 v[174:177], v229 offset:36864
	ds_read_b128 v[178:181], v229 offset:37888
	ds_read_b128 v[182:185], v229 offset:38912
	ds_read_b128 v[186:189], v229 offset:39936
	ds_read_b128 v[190:193], v229 offset:40960
	global_load_lds_dwordx4 v[210:211], off
	v_lshl_add_u64 v[208:209], s[6:7], 0, v[208:209]
	s_mov_b32 m0, s76
	s_nop 0
	global_load_lds_dwordx4 v[208:209], off
	s_waitcnt vmcnt(8)
	s_waitcnt lgkmcnt(0)
	s_barrier
	s_setprio 1
	s_waitcnt lgkmcnt(0)
	v_mfma_f32_16x16x32_bf16 v[142:145], v[60:63], v[162:165], v[142:145]
	v_mfma_f32_16x16x32_bf16 v[138:141], v[72:75], v[162:165], v[138:141]
	v_mfma_f32_16x16x32_bf16 v[126:129], v[60:63], v[170:173], v[126:129]
	v_mfma_f32_16x16x32_bf16 v[122:125], v[72:75], v[170:173], v[122:125]
	v_mfma_f32_16x16x32_bf16 v[108:111], v[60:63], v[178:181], v[108:111]
	v_mfma_f32_16x16x32_bf16 v[104:107], v[72:75], v[178:181], v[104:107]
	v_mfma_f32_16x16x32_bf16 v[92:95], v[60:63], v[186:189], v[92:95]
	v_mfma_f32_16x16x32_bf16 v[88:91], v[72:75], v[186:189], v[88:91]
	v_mfma_f32_16x16x32_bf16 v[142:145], v[64:67], v[166:169], v[142:145]
	v_mfma_f32_16x16x32_bf16 v[138:141], v[80:83], v[166:169], v[138:141]
	v_mfma_f32_16x16x32_bf16 v[126:129], v[64:67], v[174:177], v[126:129]
	v_mfma_f32_16x16x32_bf16 v[122:125], v[80:83], v[174:177], v[122:125]
	v_mfma_f32_16x16x32_bf16 v[108:111], v[64:67], v[182:185], v[108:111]
	v_mfma_f32_16x16x32_bf16 v[104:107], v[80:83], v[182:185], v[104:107]
	v_mfma_f32_16x16x32_bf16 v[92:95], v[64:67], v[190:193], v[92:95]
	v_mfma_f32_16x16x32_bf16 v[88:91], v[80:83], v[190:193], v[88:91]
	v_mfma_f32_16x16x32_bf16 v[134:137], v[146:149], v[162:165], v[134:137]
	v_mfma_f32_16x16x32_bf16 v[130:133], v[154:157], v[162:165], v[130:133]
	v_mfma_f32_16x16x32_bf16 v[118:121], v[146:149], v[170:173], v[118:121]
	v_mfma_f32_16x16x32_bf16 v[114:117], v[154:157], v[170:173], v[114:117]
	v_mfma_f32_16x16x32_bf16 v[100:103], v[146:149], v[178:181], v[100:103]
	v_mfma_f32_16x16x32_bf16 v[96:99], v[154:157], v[178:181], v[96:99]
	v_mfma_f32_16x16x32_bf16 v[84:87], v[146:149], v[186:189], v[84:87]
	v_mfma_f32_16x16x32_bf16 v[76:79], v[154:157], v[186:189], v[76:79]
	v_mfma_f32_16x16x32_bf16 v[134:137], v[150:153], v[166:169], v[134:137]
	v_mfma_f32_16x16x32_bf16 v[130:133], v[158:161], v[166:169], v[130:133]
	v_mfma_f32_16x16x32_bf16 v[118:121], v[150:153], v[174:177], v[118:121]
	v_mfma_f32_16x16x32_bf16 v[114:117], v[158:161], v[174:177], v[114:117]
	v_mfma_f32_16x16x32_bf16 v[100:103], v[150:153], v[182:185], v[100:103]
	v_mfma_f32_16x16x32_bf16 v[96:99], v[158:161], v[182:185], v[96:99]
	v_mfma_f32_16x16x32_bf16 v[84:87], v[150:153], v[190:193], v[84:87]
	v_mfma_f32_16x16x32_bf16 v[76:79], v[158:161], v[190:193], v[76:79]
	s_setprio 0
	s_barrier
	s_add_i32 s6, s30, s19
	v_lshl_add_u64 v[208:209], v[232:233], 0, s[26:27]
	s_mov_b32 m0, s6
	ds_read_b128 v[162:165], v229 offset:50176
	ds_read_b128 v[166:169], v229 offset:51200
	ds_read_b128 v[170:173], v229 offset:52224
	ds_read_b128 v[174:177], v229 offset:53248
	ds_read_b128 v[178:181], v229 offset:54272
	ds_read_b128 v[182:185], v229 offset:55296
	ds_read_b128 v[186:189], v229 offset:56320
	ds_read_b128 v[190:193], v229 offset:57344
	global_load_lds_dwordx4 v[208:209], off
	s_add_i32 m0, s6, 0x2000
	s_add_u32 s4, s4, 0x40080
	v_lshl_add_u64 v[208:209], v[234:235], 0, s[26:27]
	s_addc_u32 s5, s5, 0
	s_add_i32 s6, s31, s19
	global_load_lds_dwordx4 v[208:209], off
	v_lshl_add_u64 v[208:209], s[4:5], 0, v[194:195]
	s_mov_b32 m0, s6
	s_nop 0
	global_load_lds_dwordx4 v[208:209], off
	v_lshl_add_u64 v[208:209], s[4:5], 0, v[196:197]
	s_add_i32 m0, s6, 0x2000
	s_nop 0
	global_load_lds_dwordx4 v[208:209], off
	v_lshl_add_u64 v[208:209], v[236:237], 0, s[26:27]
	s_mov_b32 m0, s81
	s_nop 0
	global_load_lds_dwordx4 v[208:209], off
	v_lshl_add_u64 v[208:209], v[238:239], 0, s[26:27]
	s_mov_b32 m0, s82
	s_nop 0
	global_load_lds_dwordx4 v[208:209], off
	s_waitcnt vmcnt(8)
	s_waitcnt lgkmcnt(0)
	s_barrier
	s_setprio 1
	s_waitcnt lgkmcnt(0)
	v_mfma_f32_16x16x32_bf16 v[68:71], v[60:63], v[162:165], v[68:71]
	v_mfma_f32_16x16x32_bf16 v[56:59], v[72:75], v[162:165], v[56:59]
	v_mfma_f32_16x16x32_bf16 v[44:47], v[60:63], v[170:173], v[44:47]
	v_mfma_f32_16x16x32_bf16 v[40:43], v[72:75], v[170:173], v[40:43]
	v_mfma_f32_16x16x32_bf16 v[28:31], v[60:63], v[178:181], v[28:31]
	v_mfma_f32_16x16x32_bf16 v[24:27], v[72:75], v[178:181], v[24:27]
	v_mfma_f32_16x16x32_bf16 v[12:15], v[60:63], v[186:189], v[12:15]
	v_mfma_f32_16x16x32_bf16 v[8:11], v[72:75], v[186:189], v[8:11]
	v_mfma_f32_16x16x32_bf16 v[68:71], v[64:67], v[166:169], v[68:71]
	v_mfma_f32_16x16x32_bf16 v[56:59], v[80:83], v[166:169], v[56:59]
	v_mfma_f32_16x16x32_bf16 v[44:47], v[64:67], v[174:177], v[44:47]
	v_mfma_f32_16x16x32_bf16 v[40:43], v[80:83], v[174:177], v[40:43]
	v_mfma_f32_16x16x32_bf16 v[28:31], v[64:67], v[182:185], v[28:31]
	v_mfma_f32_16x16x32_bf16 v[24:27], v[80:83], v[182:185], v[24:27]
	v_mfma_f32_16x16x32_bf16 v[12:15], v[64:67], v[190:193], v[12:15]
	v_mfma_f32_16x16x32_bf16 v[8:11], v[80:83], v[190:193], v[8:11]
	v_mfma_f32_16x16x32_bf16 v[52:55], v[146:149], v[162:165], v[52:55]
	v_mfma_f32_16x16x32_bf16 v[48:51], v[154:157], v[162:165], v[48:51]
	v_mfma_f32_16x16x32_bf16 v[36:39], v[146:149], v[170:173], v[36:39]
	v_mfma_f32_16x16x32_bf16 v[32:35], v[154:157], v[170:173], v[32:35]
	v_mfma_f32_16x16x32_bf16 v[20:23], v[146:149], v[178:181], v[20:23]
	v_mfma_f32_16x16x32_bf16 v[16:19], v[154:157], v[178:181], v[16:19]
	v_mfma_f32_16x16x32_bf16 v[4:7], v[146:149], v[186:189], v[4:7]
	v_mfma_f32_16x16x32_bf16 v[0:3], v[154:157], v[186:189], v[0:3]
	v_mfma_f32_16x16x32_bf16 v[52:55], v[150:153], v[166:169], v[52:55]
	v_mfma_f32_16x16x32_bf16 v[48:51], v[158:161], v[166:169], v[48:51]
	v_mfma_f32_16x16x32_bf16 v[36:39], v[150:153], v[174:177], v[36:39]
	v_mfma_f32_16x16x32_bf16 v[32:35], v[158:161], v[174:177], v[32:35]
	v_mfma_f32_16x16x32_bf16 v[20:23], v[150:153], v[182:185], v[20:23]
	v_mfma_f32_16x16x32_bf16 v[16:19], v[158:161], v[182:185], v[16:19]
	v_mfma_f32_16x16x32_bf16 v[4:7], v[150:153], v[190:193], v[4:7]
	v_mfma_f32_16x16x32_bf16 v[0:3], v[158:161], v[190:193], v[0:3]
	s_setprio 0
	s_barrier
	s_add_i32 s24, s24, 2
	s_add_u32 s22, s22, 0x100
	s_addc_u32 s23, s23, 0
	s_add_u32 s2, s2, 0x100
	s_addc_u32 s3, s3, 0
	s_cmp_gt_u32 s24, 13
	s_cbranch_scc1 .LBB0_943

.LBB0_1586:
	s_waitcnt vmcnt(8)
	s_add_u32 s6, s2, 0x80
	s_waitcnt lgkmcnt(0)
	s_addc_u32 s7, s3, 0
	s_and_b64 s[4:5], s[4:5], exec
	s_cselect_b32 s7, s41, s7
	s_cselect_b32 s6, s40, s6
	s_cselect_b32 s5, s21, s24
	s_cselect_b32 s4, s22, s23
	s_barrier
	s_setprio 1
	s_waitcnt lgkmcnt(0)
	v_mfma_scale_f32_16x16x128_f8f6f4 v[186:189], v[24:31], v[56:63], v[186:189], v216, v216 op_sel_hi:[0,0,0]
	v_mfma_scale_f32_16x16x128_f8f6f4 v[178:181], v[16:23], v[56:63], v[178:181], v216, v216 op_sel_hi:[0,0,0]
	v_mfma_scale_f32_16x16x128_f8f6f4 v[170:173], v[24:31], v[48:55], v[170:173], v216, v216 op_sel_hi:[0,0,0]
	v_mfma_scale_f32_16x16x128_f8f6f4 v[162:165], v[16:23], v[48:55], v[162:165], v216, v216 op_sel_hi:[0,0,0]
	v_mfma_scale_f32_16x16x128_f8f6f4 v[154:157], v[24:31], v[40:47], v[154:157], v216, v216 op_sel_hi:[0,0,0]
	v_mfma_scale_f32_16x16x128_f8f6f4 v[146:149], v[16:23], v[40:47], v[146:149], v216, v216 op_sel_hi:[0,0,0]
	v_mfma_scale_f32_16x16x128_f8f6f4 v[138:141], v[24:31], v[32:39], v[138:141], v216, v216 op_sel_hi:[0,0,0]
	v_mfma_scale_f32_16x16x128_f8f6f4 v[130:133], v[16:23], v[32:39], v[130:133], v216, v216 op_sel_hi:[0,0,0]
	v_mfma_scale_f32_16x16x128_f8f6f4 v[190:193], v[0:7], v[56:63], v[190:193], v216, v216 op_sel_hi:[0,0,0]
	v_mfma_scale_f32_16x16x128_f8f6f4 v[182:185], v[8:15], v[56:63], v[182:185], v216, v216 op_sel_hi:[0,0,0]
	v_mfma_scale_f32_16x16x128_f8f6f4 v[174:177], v[0:7], v[48:55], v[174:177], v216, v216 op_sel_hi:[0,0,0]
	v_mfma_scale_f32_16x16x128_f8f6f4 v[166:169], v[8:15], v[48:55], v[166:169], v216, v216 op_sel_hi:[0,0,0]
	v_mfma_scale_f32_16x16x128_f8f6f4 v[158:161], v[0:7], v[40:47], v[158:161], v216, v216 op_sel_hi:[0,0,0]
	v_mfma_scale_f32_16x16x128_f8f6f4 v[150:153], v[8:15], v[40:47], v[150:153], v216, v216 op_sel_hi:[0,0,0]
	v_mfma_scale_f32_16x16x128_f8f6f4 v[142:145], v[0:7], v[32:39], v[142:145], v216, v216 op_sel_hi:[0,0,0]
	v_mfma_scale_f32_16x16x128_f8f6f4 v[134:137], v[8:15], v[32:39], v[134:137], v216, v216 op_sel_hi:[0,0,0]
	s_setprio 0
	s_barrier
	s_mov_b32 m0, s18
	v_lshl_add_u64 v[244:245], s[4:5], 0, v[196:197]
	s_add_u32 s78, s4, 0x20000
	ds_read_b128 v[32:35], v240 offset:17408
	ds_read_b128 v[36:39], v243 offset:17424
	ds_read_b128 v[40:43], v240 offset:19456
	ds_read_b128 v[44:47], v243 offset:19472
	ds_read_b128 v[48:51], v240 offset:21504
	ds_read_b128 v[52:55], v243 offset:21520
	ds_read_b128 v[56:59], v240 offset:23552
	ds_read_b128 v[60:63], v243 offset:23568
	global_load_lds_dwordx4 v[244:245], off
	v_lshl_add_u64 v[246:247], s[4:5], 0, v[194:195]
	s_mov_b32 m0, s19
	s_addc_u32 s79, s5, 0
	global_load_lds_dwordx4 v[246:247], off
	v_lshl_add_u64 v[248:249], s[78:79], 0, v[196:197]
	s_mov_b32 m0, s28
	v_mov_b32_e32 v201, v113
	global_load_lds_dwordx4 v[248:249], off
	v_lshl_add_u64 v[248:249], s[78:79], 0, v[194:195]
	s_mov_b32 m0, s29
	v_lshl_add_u64 v[250:251], s[6:7], 0, v[200:201]
	global_load_lds_dwordx4 v[248:249], off
	s_mov_b32 m0, s59
	v_lshl_add_u64 v[248:249], s[6:7], 0, v[112:113]
	global_load_lds_dwordx4 v112, s[6:7]
	s_mov_b32 m0, s60
	s_nop 0
	global_load_lds_dwordx4 v200, s[6:7]
	s_waitcnt vmcnt(8)
	s_waitcnt lgkmcnt(0)
	s_barrier
	s_setprio 1
	s_waitcnt lgkmcnt(0)
	v_mfma_scale_f32_16x16x128_f8f6f4 v[122:125], v[24:31], v[32:39], v[122:125], v216, v216 op_sel_hi:[0,0,0]
	v_mfma_scale_f32_16x16x128_f8f6f4 v[114:117], v[16:23], v[32:39], v[114:117], v216, v216 op_sel_hi:[0,0,0]
	v_mfma_scale_f32_16x16x128_f8f6f4 v[104:107], v[24:31], v[40:47], v[104:107], v216, v216 op_sel_hi:[0,0,0]
	v_mfma_scale_f32_16x16x128_f8f6f4 v[96:99], v[16:23], v[40:47], v[96:99], v216, v216 op_sel_hi:[0,0,0]
	v_mfma_scale_f32_16x16x128_f8f6f4 v[88:91], v[24:31], v[48:55], v[88:91], v216, v216 op_sel_hi:[0,0,0]
	v_mfma_scale_f32_16x16x128_f8f6f4 v[80:83], v[16:23], v[48:55], v[80:83], v216, v216 op_sel_hi:[0,0,0]
	v_mfma_scale_f32_16x16x128_f8f6f4 v[72:75], v[24:31], v[56:63], v[72:75], v216, v216 op_sel_hi:[0,0,0]
	v_mfma_scale_f32_16x16x128_f8f6f4 v[68:71], v[16:23], v[56:63], v[68:71], v216, v216 op_sel_hi:[0,0,0]
	v_mfma_scale_f32_16x16x128_f8f6f4 v[126:129], v[0:7], v[32:39], v[126:129], v216, v216 op_sel_hi:[0,0,0]
	v_mfma_scale_f32_16x16x128_f8f6f4 v[118:121], v[8:15], v[32:39], v[118:121], v216, v216 op_sel_hi:[0,0,0]
	v_mfma_scale_f32_16x16x128_f8f6f4 v[108:111], v[0:7], v[40:47], v[108:111], v216, v216 op_sel_hi:[0,0,0]
	v_mfma_scale_f32_16x16x128_f8f6f4 v[100:103], v[8:15], v[40:47], v[100:103], v216, v216 op_sel_hi:[0,0,0]
	v_mfma_scale_f32_16x16x128_f8f6f4 v[92:95], v[0:7], v[48:55], v[92:95], v216, v216 op_sel_hi:[0,0,0]
	v_mfma_scale_f32_16x16x128_f8f6f4 v[84:87], v[8:15], v[48:55], v[84:87], v216, v216 op_sel_hi:[0,0,0]
	v_mfma_scale_f32_16x16x128_f8f6f4 v[76:79], v[0:7], v[56:63], v[76:79], v216, v216 op_sel_hi:[0,0,0]
	v_mfma_scale_f32_16x16x128_f8f6f4 v[64:67], v[8:15], v[56:63], v[64:67], v216, v216 op_sel_hi:[0,0,0]
	s_setprio 0
	s_barrier
	ds_read_b128 v[4:7], v234
	ds_read_b128 v[8:11], v235
	ds_read_b128 v[0:3], v226
	ds_read_b128 v[16:19], v227
	ds_read_b128 v[12:15], v236
	ds_read_b128 v[20:23], v237
	ds_read_b128 v[24:27], v238
	ds_read_b128 v[28:31], v239
	s_mov_b32 m0, s61
	v_lshl_add_u64 v[210:211], s[6:7], 0, v[210:211]
	ds_read_b128 v[32:35], v240 offset:33792
	ds_read_b128 v[36:39], v243 offset:33808
	ds_read_b128 v[40:43], v240 offset:35840
	ds_read_b128 v[44:47], v243 offset:35856
	ds_read_b128 v[48:51], v240 offset:37888
	ds_read_b128 v[52:55], v243 offset:37904
	ds_read_b128 v[56:59], v240 offset:39936
	ds_read_b128 v[60:63], v243 offset:39952
	global_load_lds_dwordx4 v[210:211], off
	v_lshl_add_u64 v[208:209], s[6:7], 0, v[208:209]
	s_mov_b32 m0, s62
	s_nop 0
	global_load_lds_dwordx4 v[208:209], off
	s_waitcnt vmcnt(8)
	s_waitcnt lgkmcnt(0)
	s_barrier
	s_setprio 1
	s_waitcnt lgkmcnt(0)
	v_mfma_scale_f32_16x16x128_f8f6f4 v[186:189], v[0:7], v[32:39], v[186:189], v216, v216 op_sel_hi:[0,0,0]
	v_mfma_scale_f32_16x16x128_f8f6f4 v[178:181], v[8:15], v[32:39], v[178:181], v216, v216 op_sel_hi:[0,0,0]
	v_mfma_scale_f32_16x16x128_f8f6f4 v[170:173], v[0:7], v[40:47], v[170:173], v216, v216 op_sel_hi:[0,0,0]
	v_mfma_scale_f32_16x16x128_f8f6f4 v[162:165], v[8:15], v[40:47], v[162:165], v216, v216 op_sel_hi:[0,0,0]
	v_mfma_scale_f32_16x16x128_f8f6f4 v[154:157], v[0:7], v[48:55], v[154:157], v216, v216 op_sel_hi:[0,0,0]
	v_mfma_scale_f32_16x16x128_f8f6f4 v[146:149], v[8:15], v[48:55], v[146:149], v216, v216 op_sel_hi:[0,0,0]
	v_mfma_scale_f32_16x16x128_f8f6f4 v[138:141], v[0:7], v[56:63], v[138:141], v216, v216 op_sel_hi:[0,0,0]
	v_mfma_scale_f32_16x16x128_f8f6f4 v[130:133], v[8:15], v[56:63], v[130:133], v216, v216 op_sel_hi:[0,0,0]
	v_mfma_scale_f32_16x16x128_f8f6f4 v[190:193], v[16:23], v[32:39], v[190:193], v216, v216 op_sel_hi:[0,0,0]
	v_mfma_scale_f32_16x16x128_f8f6f4 v[182:185], v[24:31], v[32:39], v[182:185], v216, v216 op_sel_hi:[0,0,0]
	v_mfma_scale_f32_16x16x128_f8f6f4 v[174:177], v[16:23], v[40:47], v[174:177], v216, v216 op_sel_hi:[0,0,0]
	v_mfma_scale_f32_16x16x128_f8f6f4 v[166:169], v[24:31], v[40:47], v[166:169], v216, v216 op_sel_hi:[0,0,0]
	v_mfma_scale_f32_16x16x128_f8f6f4 v[158:161], v[16:23], v[48:55], v[158:161], v216, v216 op_sel_hi:[0,0,0]
	v_mfma_scale_f32_16x16x128_f8f6f4 v[150:153], v[24:31], v[48:55], v[150:153], v216, v216 op_sel_hi:[0,0,0]
	v_mfma_scale_f32_16x16x128_f8f6f4 v[142:145], v[16:23], v[56:63], v[142:145], v216, v216 op_sel_hi:[0,0,0]
	v_mfma_scale_f32_16x16x128_f8f6f4 v[134:137], v[24:31], v[56:63], v[134:137], v216, v216 op_sel_hi:[0,0,0]
	s_setprio 0
	s_barrier
	s_mov_b32 m0, s66
	v_lshl_add_u64 v[208:209], v[244:245], 0, s[26:27]
	s_add_u32 s4, s4, 0x20080
	ds_read_b128 v[32:35], v240 offset:50176
	ds_read_b128 v[36:39], v243 offset:50192
	ds_read_b128 v[40:43], v240 offset:52224
	ds_read_b128 v[44:47], v243 offset:52240
	ds_read_b128 v[48:51], v240 offset:54272
	ds_read_b128 v[52:55], v243 offset:54288
	ds_read_b128 v[56:59], v240 offset:56320
	ds_read_b128 v[60:63], v243 offset:56336
	global_load_lds_dwordx4 v[208:209], off
	v_lshl_add_u64 v[208:209], v[246:247], 0, s[26:27]
	s_mov_b32 m0, s67
	s_addc_u32 s5, s5, 0
	global_load_lds_dwordx4 v[208:209], off
	v_lshl_add_u64 v[208:209], s[4:5], 0, v[196:197]
	s_mov_b32 m0, s70
	s_nop 0
	global_load_lds_dwordx4 v[208:209], off
	v_lshl_add_u64 v[208:209], s[4:5], 0, v[194:195]
	s_mov_b32 m0, s71
	s_nop 0
	global_load_lds_dwordx4 v[208:209], off
	v_lshl_add_u64 v[208:209], v[248:249], 0, s[26:27]
	s_mov_b32 m0, s68
	s_nop 0
	global_load_lds_dwordx4 v[208:209], off
	v_lshl_add_u64 v[208:209], v[250:251], 0, s[26:27]
	s_mov_b32 m0, s69
	s_nop 0
	global_load_lds_dwordx4 v[208:209], off
	s_waitcnt vmcnt(8)
	s_waitcnt lgkmcnt(0)
	s_barrier
	s_setprio 1
	s_waitcnt lgkmcnt(0)
	v_mfma_scale_f32_16x16x128_f8f6f4 v[122:125], v[0:7], v[32:39], v[122:125], v216, v216 op_sel_hi:[0,0,0]
	v_mfma_scale_f32_16x16x128_f8f6f4 v[114:117], v[8:15], v[32:39], v[114:117], v216, v216 op_sel_hi:[0,0,0]
	v_mfma_scale_f32_16x16x128_f8f6f4 v[104:107], v[0:7], v[40:47], v[104:107], v216, v216 op_sel_hi:[0,0,0]
	v_mfma_scale_f32_16x16x128_f8f6f4 v[96:99], v[8:15], v[40:47], v[96:99], v216, v216 op_sel_hi:[0,0,0]
	v_mfma_scale_f32_16x16x128_f8f6f4 v[88:91], v[0:7], v[48:55], v[88:91], v216, v216 op_sel_hi:[0,0,0]
	v_mfma_scale_f32_16x16x128_f8f6f4 v[80:83], v[8:15], v[48:55], v[80:83], v216, v216 op_sel_hi:[0,0,0]
	v_mfma_scale_f32_16x16x128_f8f6f4 v[72:75], v[0:7], v[56:63], v[72:75], v216, v216 op_sel_hi:[0,0,0]
	v_mfma_scale_f32_16x16x128_f8f6f4 v[68:71], v[8:15], v[56:63], v[68:71], v216, v216 op_sel_hi:[0,0,0]
	v_mfma_scale_f32_16x16x128_f8f6f4 v[126:129], v[16:23], v[32:39], v[126:129], v216, v216 op_sel_hi:[0,0,0]
	v_mfma_scale_f32_16x16x128_f8f6f4 v[118:121], v[24:31], v[32:39], v[118:121], v216, v216 op_sel_hi:[0,0,0]
	v_mfma_scale_f32_16x16x128_f8f6f4 v[108:111], v[16:23], v[40:47], v[108:111], v216, v216 op_sel_hi:[0,0,0]
	v_mfma_scale_f32_16x16x128_f8f6f4 v[100:103], v[24:31], v[40:47], v[100:103], v216, v216 op_sel_hi:[0,0,0]
	v_mfma_scale_f32_16x16x128_f8f6f4 v[92:95], v[16:23], v[48:55], v[92:95], v216, v216 op_sel_hi:[0,0,0]
	v_mfma_scale_f32_16x16x128_f8f6f4 v[84:87], v[24:31], v[48:55], v[84:87], v216, v216 op_sel_hi:[0,0,0]
	v_mfma_scale_f32_16x16x128_f8f6f4 v[76:79], v[16:23], v[56:63], v[76:79], v216, v216 op_sel_hi:[0,0,0]
	v_mfma_scale_f32_16x16x128_f8f6f4 v[64:67], v[24:31], v[56:63], v[64:67], v216, v216 op_sel_hi:[0,0,0]
	s_setprio 0
	s_barrier
	s_add_i32 s30, s30, 2
	s_add_u32 s23, s23, 0x100
	s_addc_u32 s24, s24, 0
	s_add_u32 s2, s2, 0x100
	s_addc_u32 s3, s3, 0
	s_cmp_gt_u32 s30, 5
	s_cbranch_scc1 .LBB0_1589

.LBB0_1660:
	s_waitcnt vmcnt(8)
	s_add_u32 s6, s2, 0x80
	s_waitcnt lgkmcnt(0)
	s_addc_u32 s7, s3, 0
	s_and_b64 s[4:5], s[4:5], exec
	s_cselect_b32 s7, s39, s7
	s_cselect_b32 s6, s38, s6
	s_cselect_b32 s5, s21, s24
	s_cselect_b32 s4, s22, s23
	s_barrier
	s_setprio 1
	s_waitcnt lgkmcnt(0)
	v_mfma_scale_f32_16x16x128_f8f6f4 v[190:193], v[24:31], v[56:63], v[190:193], v216, v216 op_sel_hi:[0,0,0]
	v_mfma_scale_f32_16x16x128_f8f6f4 v[186:189], v[16:23], v[56:63], v[186:189], v216, v216 op_sel_hi:[0,0,0]
	v_mfma_scale_f32_16x16x128_f8f6f4 v[178:181], v[24:31], v[48:55], v[178:181], v216, v216 op_sel_hi:[0,0,0]
	v_mfma_scale_f32_16x16x128_f8f6f4 v[170:173], v[16:23], v[48:55], v[170:173], v216, v216 op_sel_hi:[0,0,0]
	v_mfma_scale_f32_16x16x128_f8f6f4 v[162:165], v[24:31], v[40:47], v[162:165], v216, v216 op_sel_hi:[0,0,0]
	v_mfma_scale_f32_16x16x128_f8f6f4 v[154:157], v[16:23], v[40:47], v[154:157], v216, v216 op_sel_hi:[0,0,0]
	v_mfma_scale_f32_16x16x128_f8f6f4 v[146:149], v[24:31], v[32:39], v[146:149], v216, v216 op_sel_hi:[0,0,0]
	v_mfma_scale_f32_16x16x128_f8f6f4 v[138:141], v[16:23], v[32:39], v[138:141], v216, v216 op_sel_hi:[0,0,0]
	v_mfma_scale_f32_16x16x128_f8f6f4 v[182:185], v[0:7], v[56:63], v[182:185], v216, v216 op_sel_hi:[0,0,0]
	v_mfma_scale_f32_16x16x128_f8f6f4 v[174:177], v[8:15], v[56:63], v[174:177], v216, v216 op_sel_hi:[0,0,0]
	v_mfma_scale_f32_16x16x128_f8f6f4 v[166:169], v[0:7], v[48:55], v[166:169], v216, v216 op_sel_hi:[0,0,0]
	v_mfma_scale_f32_16x16x128_f8f6f4 v[158:161], v[8:15], v[48:55], v[158:161], v216, v216 op_sel_hi:[0,0,0]
	v_mfma_scale_f32_16x16x128_f8f6f4 v[150:153], v[0:7], v[40:47], v[150:153], v216, v216 op_sel_hi:[0,0,0]
	v_mfma_scale_f32_16x16x128_f8f6f4 v[142:145], v[8:15], v[40:47], v[142:145], v216, v216 op_sel_hi:[0,0,0]
	v_mfma_scale_f32_16x16x128_f8f6f4 v[134:137], v[0:7], v[32:39], v[134:137], v216, v216 op_sel_hi:[0,0,0]
	v_mfma_scale_f32_16x16x128_f8f6f4 v[130:133], v[8:15], v[32:39], v[130:133], v216, v216 op_sel_hi:[0,0,0]
	s_setprio 0
	s_barrier
	s_mov_b32 m0, s28
	v_lshl_add_u64 v[250:251], s[4:5], 0, v[196:197]
	s_add_u32 s78, s4, 0x40000
	ds_read_b128 v[32:35], v246 offset:17408
	ds_read_b128 v[36:39], v235 offset:17424
	ds_read_b128 v[40:43], v246 offset:19456
	ds_read_b128 v[44:47], v235 offset:19472
	ds_read_b128 v[48:51], v246 offset:21504
	ds_read_b128 v[52:55], v235 offset:21520
	ds_read_b128 v[56:59], v246 offset:23552
	ds_read_b128 v[60:63], v235 offset:23568
	global_load_lds_dwordx4 v[250:251], off
	v_lshl_add_u64 v[252:253], s[4:5], 0, v[194:195]
	s_mov_b32 m0, s29
	s_addc_u32 s79, s5, 0
	global_load_lds_dwordx4 v[252:253], off
	v_lshl_add_u64 v[220:221], s[78:79], 0, v[196:197]
	s_mov_b32 m0, s60
	v_mov_b32_e32 v199, v113
	global_load_lds_dwordx4 v[220:221], off
	v_lshl_add_u64 v[220:221], s[78:79], 0, v[194:195]
	s_mov_b32 m0, s61
	v_lshl_add_u64 v[224:225], s[6:7], 0, v[198:199]
	global_load_lds_dwordx4 v[220:221], off
	s_mov_b32 m0, s62
	v_lshl_add_u64 v[220:221], s[6:7], 0, v[112:113]
	global_load_lds_dwordx4 v112, s[6:7]
	s_mov_b32 m0, s63
	s_nop 0
	global_load_lds_dwordx4 v198, s[6:7]
	s_waitcnt vmcnt(8)
	s_waitcnt lgkmcnt(0)
	s_barrier
	s_setprio 1
	s_waitcnt lgkmcnt(0)
	v_mfma_scale_f32_16x16x128_f8f6f4 v[126:129], v[24:31], v[32:39], v[126:129], v216, v216 op_sel_hi:[0,0,0]
	v_mfma_scale_f32_16x16x128_f8f6f4 v[122:125], v[16:23], v[32:39], v[122:125], v216, v216 op_sel_hi:[0,0,0]
	v_mfma_scale_f32_16x16x128_f8f6f4 v[114:117], v[24:31], v[40:47], v[114:117], v216, v216 op_sel_hi:[0,0,0]
	v_mfma_scale_f32_16x16x128_f8f6f4 v[104:107], v[16:23], v[40:47], v[104:107], v216, v216 op_sel_hi:[0,0,0]
	v_mfma_scale_f32_16x16x128_f8f6f4 v[96:99], v[24:31], v[48:55], v[96:99], v216, v216 op_sel_hi:[0,0,0]
	v_mfma_scale_f32_16x16x128_f8f6f4 v[88:91], v[16:23], v[48:55], v[88:91], v216, v216 op_sel_hi:[0,0,0]
	v_mfma_scale_f32_16x16x128_f8f6f4 v[80:83], v[24:31], v[56:63], v[80:83], v216, v216 op_sel_hi:[0,0,0]
	v_mfma_scale_f32_16x16x128_f8f6f4 v[72:75], v[16:23], v[56:63], v[72:75], v216, v216 op_sel_hi:[0,0,0]
	v_mfma_scale_f32_16x16x128_f8f6f4 v[118:121], v[0:7], v[32:39], v[118:121], v216, v216 op_sel_hi:[0,0,0]
	v_mfma_scale_f32_16x16x128_f8f6f4 v[108:111], v[8:15], v[32:39], v[108:111], v216, v216 op_sel_hi:[0,0,0]
	v_mfma_scale_f32_16x16x128_f8f6f4 v[100:103], v[0:7], v[40:47], v[100:103], v216, v216 op_sel_hi:[0,0,0]
	v_mfma_scale_f32_16x16x128_f8f6f4 v[92:95], v[8:15], v[40:47], v[92:95], v216, v216 op_sel_hi:[0,0,0]
	v_mfma_scale_f32_16x16x128_f8f6f4 v[84:87], v[0:7], v[48:55], v[84:87], v216, v216 op_sel_hi:[0,0,0]
	v_mfma_scale_f32_16x16x128_f8f6f4 v[76:79], v[8:15], v[48:55], v[76:79], v216, v216 op_sel_hi:[0,0,0]
	v_mfma_scale_f32_16x16x128_f8f6f4 v[68:71], v[0:7], v[56:63], v[68:71], v216, v216 op_sel_hi:[0,0,0]
	v_mfma_scale_f32_16x16x128_f8f6f4 v[64:67], v[8:15], v[56:63], v[64:67], v216, v216 op_sel_hi:[0,0,0]
	s_setprio 0
	s_barrier
	ds_read_b128 v[4:7], v240
	ds_read_b128 v[8:11], v241
	ds_read_b128 v[0:3], v232
	ds_read_b128 v[16:19], v233
	ds_read_b128 v[12:15], v242
	ds_read_b128 v[20:23], v243
	ds_read_b128 v[24:27], v244
	ds_read_b128 v[28:31], v245
	s_mov_b32 m0, s64
	v_lshl_add_u64 v[210:211], s[6:7], 0, v[210:211]
	ds_read_b128 v[32:35], v246 offset:33792
	ds_read_b128 v[36:39], v235 offset:33808
	ds_read_b128 v[40:43], v246 offset:35840
	ds_read_b128 v[44:47], v235 offset:35856
	ds_read_b128 v[48:51], v246 offset:37888
	ds_read_b128 v[52:55], v235 offset:37904
	ds_read_b128 v[56:59], v246 offset:39936
	ds_read_b128 v[60:63], v235 offset:39952
	global_load_lds_dwordx4 v[210:211], off
	v_lshl_add_u64 v[208:209], s[6:7], 0, v[208:209]
	s_mov_b32 m0, s65
	s_nop 0
	global_load_lds_dwordx4 v[208:209], off
	s_waitcnt vmcnt(8)
	s_waitcnt lgkmcnt(0)
	s_barrier
	s_setprio 1
	s_waitcnt lgkmcnt(0)
	v_mfma_scale_f32_16x16x128_f8f6f4 v[190:193], v[0:7], v[32:39], v[190:193], v216, v216 op_sel_hi:[0,0,0]
	v_mfma_scale_f32_16x16x128_f8f6f4 v[186:189], v[8:15], v[32:39], v[186:189], v216, v216 op_sel_hi:[0,0,0]
	v_mfma_scale_f32_16x16x128_f8f6f4 v[178:181], v[0:7], v[40:47], v[178:181], v216, v216 op_sel_hi:[0,0,0]
	v_mfma_scale_f32_16x16x128_f8f6f4 v[170:173], v[8:15], v[40:47], v[170:173], v216, v216 op_sel_hi:[0,0,0]
	v_mfma_scale_f32_16x16x128_f8f6f4 v[162:165], v[0:7], v[48:55], v[162:165], v216, v216 op_sel_hi:[0,0,0]
	v_mfma_scale_f32_16x16x128_f8f6f4 v[154:157], v[8:15], v[48:55], v[154:157], v216, v216 op_sel_hi:[0,0,0]
	v_mfma_scale_f32_16x16x128_f8f6f4 v[146:149], v[0:7], v[56:63], v[146:149], v216, v216 op_sel_hi:[0,0,0]
	v_mfma_scale_f32_16x16x128_f8f6f4 v[138:141], v[8:15], v[56:63], v[138:141], v216, v216 op_sel_hi:[0,0,0]
	v_mfma_scale_f32_16x16x128_f8f6f4 v[182:185], v[16:23], v[32:39], v[182:185], v216, v216 op_sel_hi:[0,0,0]
	v_mfma_scale_f32_16x16x128_f8f6f4 v[174:177], v[24:31], v[32:39], v[174:177], v216, v216 op_sel_hi:[0,0,0]
	v_mfma_scale_f32_16x16x128_f8f6f4 v[166:169], v[16:23], v[40:47], v[166:169], v216, v216 op_sel_hi:[0,0,0]
	v_mfma_scale_f32_16x16x128_f8f6f4 v[158:161], v[24:31], v[40:47], v[158:161], v216, v216 op_sel_hi:[0,0,0]
	v_mfma_scale_f32_16x16x128_f8f6f4 v[150:153], v[16:23], v[48:55], v[150:153], v216, v216 op_sel_hi:[0,0,0]
	v_mfma_scale_f32_16x16x128_f8f6f4 v[142:145], v[24:31], v[48:55], v[142:145], v216, v216 op_sel_hi:[0,0,0]
	v_mfma_scale_f32_16x16x128_f8f6f4 v[134:137], v[16:23], v[56:63], v[134:137], v216, v216 op_sel_hi:[0,0,0]
	v_mfma_scale_f32_16x16x128_f8f6f4 v[130:133], v[24:31], v[56:63], v[130:133], v216, v216 op_sel_hi:[0,0,0]
	s_setprio 0
	s_barrier
	s_mov_b32 m0, s69
	v_lshl_add_u64 v[208:209], v[250:251], 0, s[26:27]
	s_add_u32 s4, s4, 0x40080
	ds_read_b128 v[32:35], v246 offset:50176
	ds_read_b128 v[36:39], v235 offset:50192
	ds_read_b128 v[40:43], v246 offset:52224
	ds_read_b128 v[44:47], v235 offset:52240
	ds_read_b128 v[48:51], v246 offset:54272
	ds_read_b128 v[52:55], v235 offset:54288
	ds_read_b128 v[56:59], v246 offset:56320
	ds_read_b128 v[60:63], v235 offset:56336
	global_load_lds_dwordx4 v[208:209], off
	v_lshl_add_u64 v[208:209], v[252:253], 0, s[26:27]
	s_mov_b32 m0, s70
	s_addc_u32 s5, s5, 0
	global_load_lds_dwordx4 v[208:209], off
	v_lshl_add_u64 v[208:209], s[4:5], 0, v[196:197]
	s_mov_b32 m0, s73
	s_nop 0
	global_load_lds_dwordx4 v[208:209], off
	v_lshl_add_u64 v[208:209], s[4:5], 0, v[194:195]
	s_mov_b32 m0, s74
	s_nop 0
	global_load_lds_dwordx4 v[208:209], off
	v_lshl_add_u64 v[208:209], v[220:221], 0, s[26:27]
	s_mov_b32 m0, s71
	s_nop 0
	global_load_lds_dwordx4 v[208:209], off
	v_lshl_add_u64 v[208:209], v[224:225], 0, s[26:27]
	s_mov_b32 m0, s72
	s_nop 0
	global_load_lds_dwordx4 v[208:209], off
	s_waitcnt vmcnt(8)
	s_waitcnt lgkmcnt(0)
	s_barrier
	s_setprio 1
	s_waitcnt lgkmcnt(0)
	v_mfma_scale_f32_16x16x128_f8f6f4 v[126:129], v[0:7], v[32:39], v[126:129], v216, v216 op_sel_hi:[0,0,0]
	v_mfma_scale_f32_16x16x128_f8f6f4 v[122:125], v[8:15], v[32:39], v[122:125], v216, v216 op_sel_hi:[0,0,0]
	v_mfma_scale_f32_16x16x128_f8f6f4 v[114:117], v[0:7], v[40:47], v[114:117], v216, v216 op_sel_hi:[0,0,0]
	v_mfma_scale_f32_16x16x128_f8f6f4 v[104:107], v[8:15], v[40:47], v[104:107], v216, v216 op_sel_hi:[0,0,0]
	v_mfma_scale_f32_16x16x128_f8f6f4 v[96:99], v[0:7], v[48:55], v[96:99], v216, v216 op_sel_hi:[0,0,0]
	v_mfma_scale_f32_16x16x128_f8f6f4 v[88:91], v[8:15], v[48:55], v[88:91], v216, v216 op_sel_hi:[0,0,0]
	v_mfma_scale_f32_16x16x128_f8f6f4 v[80:83], v[0:7], v[56:63], v[80:83], v216, v216 op_sel_hi:[0,0,0]
	v_mfma_scale_f32_16x16x128_f8f6f4 v[72:75], v[8:15], v[56:63], v[72:75], v216, v216 op_sel_hi:[0,0,0]
	v_mfma_scale_f32_16x16x128_f8f6f4 v[118:121], v[16:23], v[32:39], v[118:121], v216, v216 op_sel_hi:[0,0,0]
	v_mfma_scale_f32_16x16x128_f8f6f4 v[108:111], v[24:31], v[32:39], v[108:111], v216, v216 op_sel_hi:[0,0,0]
	v_mfma_scale_f32_16x16x128_f8f6f4 v[100:103], v[16:23], v[40:47], v[100:103], v216, v216 op_sel_hi:[0,0,0]
	v_mfma_scale_f32_16x16x128_f8f6f4 v[92:95], v[24:31], v[40:47], v[92:95], v216, v216 op_sel_hi:[0,0,0]
	v_mfma_scale_f32_16x16x128_f8f6f4 v[84:87], v[16:23], v[48:55], v[84:87], v216, v216 op_sel_hi:[0,0,0]
	v_mfma_scale_f32_16x16x128_f8f6f4 v[76:79], v[24:31], v[48:55], v[76:79], v216, v216 op_sel_hi:[0,0,0]
	v_mfma_scale_f32_16x16x128_f8f6f4 v[68:71], v[16:23], v[56:63], v[68:71], v216, v216 op_sel_hi:[0,0,0]
	v_mfma_scale_f32_16x16x128_f8f6f4 v[64:67], v[24:31], v[56:63], v[64:67], v216, v216 op_sel_hi:[0,0,0]
	s_setprio 0
	s_barrier
	s_add_i32 s30, s30, 2
	s_add_u32 s23, s23, 0x100
	s_addc_u32 s24, s24, 0
	s_add_u32 s2, s2, 0x100
	s_addc_u32 s3, s3, 0
	s_cmp_gt_u32 s30, 13
	s_cbranch_scc1 .LBB0_1663
